# P9 activation stores widened: 8 dwordx2 -> 4 dwordx4 via permlane16_swap (same bytes), relaxed peel waits vmcnt(12)
# baseline (speedup 1.0000x reference)
.Lp9_pw1:
	s_waitcnt vmcnt(12)
	s_waitcnt lgkmcnt(0)
	s_barrier
	s_setprio 1
	s_waitcnt lgkmcnt(0)
	v_mfma_f32_16x16x128_f8f6f4 v[158:161], v[18:25], v[174:181], 0
	v_mfma_f32_16x16x128_f8f6f4 v[154:157], v[26:33], v[174:181], 0
	v_mfma_f32_16x16x128_f8f6f4 v[142:145], v[18:25], v[198:205], 0
	v_mfma_f32_16x16x128_f8f6f4 v[134:137], v[26:33], v[198:205], 0
	v_mfma_f32_16x16x128_f8f6f4 v[126:129], v[18:25], v[206:213], 0
	v_mfma_f32_16x16x128_f8f6f4 v[118:121], v[26:33], v[206:213], 0
	v_mfma_f32_16x16x128_f8f6f4 v[110:113], v[18:25], v[214:221], 0
	v_mfma_f32_16x16x128_f8f6f4 v[102:105], v[26:33], v[214:221], 0
	s_setprio 0
	s_setprio 1
	v_mfma_f32_16x16x128_f8f6f4 v[150:153], v[2:9], v[174:181], 0
	v_mfma_f32_16x16x128_f8f6f4 v[146:149], v[10:17], v[174:181], 0
	v_mfma_f32_16x16x128_f8f6f4 v[138:141], v[2:9], v[198:205], 0
	v_mfma_f32_16x16x128_f8f6f4 v[130:133], v[10:17], v[198:205], 0
	v_mfma_f32_16x16x128_f8f6f4 v[122:125], v[2:9], v[206:213], 0
	v_mfma_f32_16x16x128_f8f6f4 v[114:117], v[10:17], v[206:213], 0
	v_mfma_f32_16x16x128_f8f6f4 v[106:109], v[2:9], v[214:221], 0
	v_mfma_f32_16x16x128_f8f6f4 v[98:101], v[10:17], v[214:221], 0
	s_setprio 0
	s_barrier
	s_add_i32 s37, s85, s58
	v_lshl_add_u64 v[174:175], s[46:47], 0, v[164:165]
	s_mov_b32 m0, s37
	ds_read_b128 v[198:201], v188 offset:16384
	ds_read_b128 v[202:205], v188 offset:17408
	ds_read_b128 v[206:209], v188 offset:18432
	ds_read_b128 v[210:213], v188 offset:19456
	ds_read_b128 v[214:217], v188 offset:20480
	ds_read_b128 v[218:221], v188 offset:21504
	ds_read_b128 v[222:225], v188 offset:22528
	ds_read_b128 v[226:229], v188 offset:23552
	global_load_lds_dwordx4 v[174:175], off
	s_add_i32 m0, s37, 0x2000
	s_add_u32 s50, s46, 0x40000
	v_lshl_add_u64 v[176:177], s[46:47], 0, v[166:167]
	s_addc_u32 s51, s47, 0
	s_add_i32 s37, s86, s58
	global_load_lds_dwordx4 v[176:177], off
	v_lshl_add_u64 v[178:179], s[50:51], 0, v[164:165]
	s_mov_b32 m0, s37
	v_cndmask_b32_e64 v162, v196, v192, s[6:7]
	global_load_lds_dwordx4 v[178:179], off
	v_lshl_add_u64 v[178:179], s[50:51], 0, v[166:167]
	s_add_i32 m0, s37, 0x2000
	s_nop 0
	global_load_lds_dwordx4 v[178:179], off
	s_mov_b32 m0, s59
	v_lshl_add_u64 v[178:179], s[48:49], 0, v[162:163]
	global_load_lds_dwordx4 v162, s[48:49]
	v_cndmask_b32_e64 v162, v170, v191, s[6:7]
	s_mov_b32 m0, s60
	v_lshl_add_u64 v[180:181], s[48:49], 0, v[162:163]
	global_load_lds_dwordx4 v162, s[48:49]
	s_cmp_lt_u32 s63, 2
	s_cbranch_scc0 .Lp9_pw2
	s_waitcnt vmcnt(8)
.Lp9_pw2:
	s_waitcnt vmcnt(12)
	s_waitcnt lgkmcnt(0)
	s_barrier
	s_setprio 1
	s_waitcnt lgkmcnt(0)
	v_mfma_f32_16x16x128_f8f6f4 v[94:97], v[18:25], v[198:205], 0
	v_mfma_f32_16x16x128_f8f6f4 v[86:89], v[26:33], v[198:205], 0
	v_mfma_f32_16x16x128_f8f6f4 v[78:81], v[18:25], v[206:213], 0
	v_mfma_f32_16x16x128_f8f6f4 v[70:73], v[26:33], v[206:213], 0
	v_mfma_f32_16x16x128_f8f6f4 v[62:65], v[18:25], v[214:221], 0
	v_mfma_f32_16x16x128_f8f6f4 v[54:57], v[26:33], v[214:221], 0
	v_mfma_f32_16x16x128_f8f6f4 v[46:49], v[18:25], v[222:229], 0
	v_mfma_f32_16x16x128_f8f6f4 v[38:41], v[26:33], v[222:229], 0
	s_setprio 0
	s_setprio 1
	v_mfma_f32_16x16x128_f8f6f4 v[90:93], v[2:9], v[198:205], 0
	v_mfma_f32_16x16x128_f8f6f4 v[82:85], v[10:17], v[198:205], 0
	v_mfma_f32_16x16x128_f8f6f4 v[74:77], v[2:9], v[206:213], 0
	v_mfma_f32_16x16x128_f8f6f4 v[66:69], v[10:17], v[206:213], 0
	v_mfma_f32_16x16x128_f8f6f4 v[58:61], v[2:9], v[214:221], 0
	v_mfma_f32_16x16x128_f8f6f4 v[50:53], v[10:17], v[214:221], 0
	v_mfma_f32_16x16x128_f8f6f4 v[42:45], v[2:9], v[222:229], 0
	v_mfma_f32_16x16x128_f8f6f4 v[34:37], v[10:17], v[222:229], 0
	s_setprio 0
	s_barrier
	s_add_i32 s37, 0, 0x18000
	s_add_i32 s50, 0, 0x1c000
	v_add_u32_e32 v14, s37, v185
	v_add_u32_e32 v30, s50, v185
	ds_read_b128 v[2:5], v14
	ds_read_b128 v[6:9], v14 offset:1024
	ds_read_b128 v[10:13], v14 offset:2048
	ds_read_b128 v[14:17], v14 offset:3072
	ds_read_b128 v[18:21], v30
	ds_read_b128 v[22:25], v30 offset:1024
	ds_read_b128 v[26:29], v30 offset:2048
	ds_read_b128 v[30:33], v30 offset:3072
	s_mov_b32 m0, s61
	v_cndmask_b32_e64 v162, v168, v190, s[6:7]
	ds_read_b128 v[198:201], v188 offset:32768
	ds_read_b128 v[202:205], v188 offset:33792
	ds_read_b128 v[206:209], v188 offset:34816
	ds_read_b128 v[210:213], v188 offset:35840
	ds_read_b128 v[214:217], v188 offset:36864
	ds_read_b128 v[218:221], v188 offset:37888
	ds_read_b128 v[222:225], v188 offset:38912
	ds_read_b128 v[226:229], v188 offset:39936
	global_load_lds_dwordx4 v162, s[48:49]
	v_cndmask_b32_e64 v162, v172, v193, s[6:7]
	s_mov_b32 m0, s62
	s_nop 0
	global_load_lds_dwordx4 v162, s[48:49]
	s_waitcnt vmcnt(8)
	s_waitcnt lgkmcnt(0)
	s_barrier
	s_setprio 1
	s_waitcnt lgkmcnt(0)
	v_mfma_f32_16x16x128_f8f6f4 v[158:161], v[2:9], v[198:205], v[158:161]
	v_mfma_f32_16x16x128_f8f6f4 v[154:157], v[10:17], v[198:205], v[154:157]
	v_mfma_f32_16x16x128_f8f6f4 v[142:145], v[2:9], v[206:213], v[142:145]
	v_mfma_f32_16x16x128_f8f6f4 v[134:137], v[10:17], v[206:213], v[134:137]
	v_mfma_f32_16x16x128_f8f6f4 v[126:129], v[2:9], v[214:221], v[126:129]
	v_mfma_f32_16x16x128_f8f6f4 v[118:121], v[10:17], v[214:221], v[118:121]
	v_mfma_f32_16x16x128_f8f6f4 v[110:113], v[2:9], v[222:229], v[110:113]
	v_mfma_f32_16x16x128_f8f6f4 v[102:105], v[10:17], v[222:229], v[102:105]
	s_setprio 0
	s_setprio 1
	v_mfma_f32_16x16x128_f8f6f4 v[150:153], v[18:25], v[198:205], v[150:153]
	v_mfma_f32_16x16x128_f8f6f4 v[146:149], v[26:33], v[198:205], v[146:149]
	v_mfma_f32_16x16x128_f8f6f4 v[138:141], v[18:25], v[206:213], v[138:141]
	v_mfma_f32_16x16x128_f8f6f4 v[130:133], v[26:33], v[206:213], v[130:133]
	v_mfma_f32_16x16x128_f8f6f4 v[122:125], v[18:25], v[214:221], v[122:125]
	v_mfma_f32_16x16x128_f8f6f4 v[114:117], v[26:33], v[214:221], v[114:117]
	v_mfma_f32_16x16x128_f8f6f4 v[106:109], v[18:25], v[222:229], v[106:109]
	v_mfma_f32_16x16x128_f8f6f4 v[98:101], v[26:33], v[222:229], v[98:101]
	s_setprio 0
	s_barrier
	s_add_i32 s6, s37, s58
	v_lshl_add_u64 v[174:175], v[174:175], 0, s[16:17]
	s_mov_b32 m0, s6
	ds_read_b128 v[198:201], v188 offset:49152
	ds_read_b128 v[202:205], v188 offset:50176
	ds_read_b128 v[206:209], v188 offset:51200
	ds_read_b128 v[210:213], v188 offset:52224
	ds_read_b128 v[214:217], v188 offset:53248
	ds_read_b128 v[218:221], v188 offset:54272
	ds_read_b128 v[222:225], v188 offset:55296
	ds_read_b128 v[226:229], v188 offset:56320
	global_load_lds_dwordx4 v[174:175], off
	s_add_i32 m0, s6, 0x2000
	s_add_u32 s6, s46, 0x40080
	v_lshl_add_u64 v[174:175], v[176:177], 0, s[16:17]
	s_addc_u32 s7, s47, 0
	s_add_i32 s37, s50, s58
	global_load_lds_dwordx4 v[174:175], off
	v_lshl_add_u64 v[174:175], s[6:7], 0, v[164:165]
	s_mov_b32 m0, s37
	s_nop 0
	global_load_lds_dwordx4 v[174:175], off
	v_lshl_add_u64 v[174:175], s[6:7], 0, v[166:167]
	s_add_i32 m0, s37, 0x2000
	s_nop 0
	global_load_lds_dwordx4 v[174:175], off
	v_lshl_add_u64 v[174:175], v[178:179], 0, s[16:17]
	s_mov_b32 m0, s66
	s_nop 0
	global_load_lds_dwordx4 v[174:175], off
	v_lshl_add_u64 v[174:175], v[180:181], 0, s[16:17]
	s_mov_b32 m0, s67
	s_nop 0
	global_load_lds_dwordx4 v[174:175], off
	s_waitcnt vmcnt(8)
	s_waitcnt lgkmcnt(0)
	s_barrier
	s_setprio 1
	s_waitcnt lgkmcnt(0)
	v_mfma_f32_16x16x128_f8f6f4 v[94:97], v[2:9], v[198:205], v[94:97]
	v_mfma_f32_16x16x128_f8f6f4 v[86:89], v[10:17], v[198:205], v[86:89]
	v_mfma_f32_16x16x128_f8f6f4 v[78:81], v[2:9], v[206:213], v[78:81]
	v_mfma_f32_16x16x128_f8f6f4 v[70:73], v[10:17], v[206:213], v[70:73]
	v_mfma_f32_16x16x128_f8f6f4 v[62:65], v[2:9], v[214:221], v[62:65]
	v_mfma_f32_16x16x128_f8f6f4 v[54:57], v[10:17], v[214:221], v[54:57]
	v_mfma_f32_16x16x128_f8f6f4 v[46:49], v[2:9], v[222:229], v[46:49]
	v_mfma_f32_16x16x128_f8f6f4 v[38:41], v[10:17], v[222:229], v[38:41]
	s_setprio 0
	s_setprio 1
	v_mfma_f32_16x16x128_f8f6f4 v[90:93], v[18:25], v[198:205], v[90:93]
	v_mfma_f32_16x16x128_f8f6f4 v[82:85], v[26:33], v[198:205], v[82:85]
	v_mfma_f32_16x16x128_f8f6f4 v[74:77], v[18:25], v[206:213], v[74:77]
	v_mfma_f32_16x16x128_f8f6f4 v[66:69], v[26:33], v[206:213], v[66:69]
	v_mfma_f32_16x16x128_f8f6f4 v[58:61], v[18:25], v[214:221], v[58:61]
	v_mfma_f32_16x16x128_f8f6f4 v[50:53], v[26:33], v[214:221], v[50:53]
	v_mfma_f32_16x16x128_f8f6f4 v[42:45], v[18:25], v[222:229], v[42:45]
	v_mfma_f32_16x16x128_f8f6f4 v[34:37], v[26:33], v[222:229], v[34:37]
	s_setprio 0
	s_barrier
	s_add_i32 s29, s29, 2
	s_add_u32 s44, s44, 0x100
	s_addc_u32 s45, s45, 0
	s_add_u32 s38, s38, 0x100
	s_addc_u32 s39, s39, 0
	s_cmp_gt_u32 s29, 13
	s_cbranch_scc1 .LBB0_1368
	s_branch .LBB0_1356

.LBB0_1370:
	s_ashr_i32 s37, s36, 31
	s_lshl_b64 s[6:7], s[36:37], 14
	v_lshl_or_b32 v22, s34, 7, v186
	s_add_u32 s6, s10, s6
	s_addc_u32 s7, s11, s7
	v_ashrrev_i32_e32 v23, 31, v22
	v_bfe_u32 v250, v186, 3, 1
	v_mul_u32_u24_e32 v250, 0x7ff8, v250
	v_add_u32_e32 v22, v22, v250
	s_mov_b64 s[6:7], 0x2000
	v_lshl_add_u32 v18, v195, 8, v171
	v_or_b32_e32 v24, 16, v18
	v_or_b32_e32 v26, 32, v18
	v_or_b32_e32 v28, 48, v18
	v_ashrrev_i32_e32 v19, 31, v18
	v_ashrrev_i32_e32 v25, 31, v24
	v_ashrrev_i32_e32 v27, 31, v26
	v_ashrrev_i32_e32 v29, 31, v28
	v_lshlrev_b64 v[18:19], 11, v[18:19]
	v_lshlrev_b64 v[24:25], 11, v[24:25]
	v_lshlrev_b64 v[26:27], 11, v[26:27]
	v_lshlrev_b64 v[28:29], 11, v[28:29]
	v_lshl_add_u64 v[18:19], s[14:15], 0, v[18:19]
	v_lshl_add_u64 v[24:25], s[14:15], 0, v[24:25]
	v_lshl_add_u64 v[26:27], s[14:15], 0, v[26:27]
	v_lshl_add_u64 v[28:29], s[14:15], 0, v[28:29]
	v_lshl_add_u64 v[18:19], v[18:19], 0, v[22:23]
	v_lshl_add_u64 v[24:25], v[24:25], 0, v[22:23]
	v_lshl_add_u64 v[26:27], v[26:27], 0, v[22:23]
	v_lshl_add_u64 v[22:23], v[28:29], 0, v[22:23]
	v_mov_b32_e32 v20, v163
	v_mov_b32_e32 v21, v163
	s_mov_b32 s6, 0x40000
	v_mov_b64_e32 v[6:7], v[234:235]
	v_mov_b64_e32 v[8:9], v[236:237]
	v_mov_b64_e32 v[14:15], v[238:239]
	v_mov_b64_e32 v[16:17], v[240:241]
	v_mov_b64_e32 v[10:11], v[242:243]
	v_mov_b64_e32 v[12:13], v[244:245]
	v_mov_b64_e32 v[2:3], v[246:247]
	v_mov_b64_e32 v[4:5], v[248:249]
	v_pk_fma_f32 v[32:33], v[154:155], s[22:23], v[6:7] op_sel_hi:[1,0,1]
	v_pk_fma_f32 v[28:29], v[158:159], s[22:23], v[14:15] op_sel_hi:[1,0,1]
	v_pk_fma_f32 v[154:155], v[156:157], s[22:23], v[8:9] op_sel_hi:[1,0,1]
	v_min_f32_e32 v28, 0x40e00000, v28
	v_min_f32_e32 v29, 0x40e00000, v29
	v_min_f32_e32 v32, 0x40e00000, v32
	v_min_f32_e32 v33, 0x40e00000, v33
	v_pk_mul_f32 v[156:157], v[28:29], s[24:25] op_sel_hi:[1,0]
	v_pk_fma_f32 v[30:31], v[160:161], s[22:23], v[16:17] op_sel_hi:[1,0,1]
	v_pk_mul_f32 v[160:161], v[32:33], s[24:25] op_sel_hi:[1,0]
	v_exp_f32_e32 v156, v156
	v_exp_f32_e32 v157, v157
	v_exp_f32_e32 v160, v160
	v_exp_f32_e32 v161, v161
	v_min_f32_e32 v30, 0x40e00000, v30
	v_min_f32_e32 v31, 0x40e00000, v31
	v_min_f32_e32 v154, 0x40e00000, v154
	v_min_f32_e32 v155, 0x40e00000, v155
	v_pk_mul_f32 v[158:159], v[30:31], s[24:25] op_sel_hi:[1,0]
	v_pk_mul_f32 v[168:169], v[154:155], s[24:25] op_sel_hi:[1,0]
	v_exp_f32_e32 v158, v158
	v_exp_f32_e32 v159, v159
	v_pk_add_f32 v[156:157], v[156:157], 1.0 op_sel_hi:[1,0]
	v_exp_f32_e32 v168, v168
	v_exp_f32_e32 v169, v169
	v_pk_add_f32 v[160:161], v[160:161], 1.0 op_sel_hi:[1,0]
	v_rcp_f32_e32 v156, v156
	v_rcp_f32_e32 v157, v157
	v_rcp_f32_e32 v160, v160
	v_rcp_f32_e32 v161, v161
	v_pk_fma_f32 v[150:151], v[150:151], s[22:23], v[10:11] op_sel_hi:[1,0,1]
	v_pk_fma_f32 v[146:147], v[146:147], s[22:23], v[2:3] op_sel_hi:[1,0,1]
	v_med3_f32 v150, v150, s87, v189
	v_med3_f32 v151, v151, s87, v189
	v_pk_add_f32 v[158:159], v[158:159], 1.0 op_sel_hi:[1,0]
	v_med3_f32 v146, v146, s87, v189
	v_med3_f32 v147, v147, s87, v189
	v_pk_add_f32 v[150:151], v[150:151], 1.0 op_sel_hi:[1,0]
	v_pk_add_f32 v[168:169], v[168:169], 1.0 op_sel_hi:[1,0]
	v_rcp_f32_e32 v158, v158
	v_rcp_f32_e32 v159, v159
	v_pk_mul_f32 v[28:29], v[28:29], v[156:157]
	v_pk_add_f32 v[146:147], v[146:147], 1.0 op_sel_hi:[1,0]
	v_rcp_f32_e32 v168, v168
	v_rcp_f32_e32 v169, v169
	v_pk_mul_f32 v[32:33], v[32:33], v[160:161]
	v_pk_mul_f32 v[28:29], v[150:151], v[28:29]
	v_pk_fma_f32 v[152:153], v[152:153], s[22:23], v[12:13] op_sel_hi:[1,0,1]
	v_pk_mul_f32 v[32:33], v[146:147], v[32:33]
	v_cvt_pk_fp8_f32 v20, v28, v29
	v_pk_fma_f32 v[148:149], v[148:149], s[22:23], v[4:5] op_sel_hi:[1,0,1]
	v_med3_f32 v152, v152, s87, v189
	v_med3_f32 v153, v153, s87, v189
	v_cvt_pk_fp8_f32 v21, v32, v33
	v_med3_f32 v148, v148, s87, v189
	v_med3_f32 v149, v149, s87, v189
	v_pk_add_f32 v[152:153], v[152:153], 1.0 op_sel_hi:[1,0]
	v_pk_mul_f32 v[30:31], v[30:31], v[158:159]
	v_pk_fma_f32 v[142:143], v[142:143], s[22:23], v[14:15] op_sel_hi:[1,0,1]
	v_pk_add_f32 v[148:149], v[148:149], 1.0 op_sel_hi:[1,0]
	v_pk_mul_f32 v[154:155], v[154:155], v[168:169]
	v_pk_mul_f32 v[28:29], v[152:153], v[30:31]
	v_pk_mul_f32 v[30:31], v[148:149], v[154:155]
	v_cvt_pk_fp8_f32 v20, v28, v29 op_sel:[0,0,1]
	v_min_f32_e32 v28, 0x40e00000, v142
	v_min_f32_e32 v29, 0x40e00000, v143
	v_cvt_pk_fp8_f32 v21, v30, v31 op_sel:[0,0,1]
	v_pk_mul_f32 v[30:31], v[28:29], s[24:25] op_sel_hi:[1,0]
	v_pk_fma_f32 v[32:33], v[138:139], s[22:23], v[10:11] op_sel_hi:[1,0,1]
	v_exp_f32_e32 v30, v30
	v_exp_f32_e32 v31, v31
	v_pk_fma_f32 v[138:139], v[144:145], s[22:23], v[16:17] op_sel_hi:[1,0,1]
	v_med3_f32 v32, v32, s87, v189
	v_min_f32_e32 v138, 0x40e00000, v138
	v_pk_add_f32 v[30:31], v[30:31], 1.0 op_sel_hi:[1,0]
	v_min_f32_e32 v139, 0x40e00000, v139
	v_rcp_f32_e32 v30, v30
	v_rcp_f32_e32 v31, v31
	v_pk_mul_f32 v[142:143], v[138:139], s[24:25] op_sel_hi:[1,0]
	v_med3_f32 v33, v33, s87, v189
	v_exp_f32_e32 v142, v142
	v_exp_f32_e32 v143, v143
	v_pk_mul_f32 v[28:29], v[28:29], v[30:31]
	v_pk_add_f32 v[30:31], v[32:33], 1.0 op_sel_hi:[1,0]
	v_pk_fma_f32 v[32:33], v[140:141], s[22:23], v[12:13] op_sel_hi:[1,0,1]
	v_pk_mul_f32 v[30:31], v[30:31], v[28:29]
	v_pk_add_f32 v[28:29], v[142:143], 1.0 op_sel_hi:[1,0]
	v_med3_f32 v32, v32, s87, v189
	v_rcp_f32_e32 v28, v28
	v_rcp_f32_e32 v29, v29
	v_med3_f32 v33, v33, s87, v189
	v_pk_add_f32 v[32:33], v[32:33], 1.0 op_sel_hi:[1,0]
	v_pk_fma_f32 v[136:137], v[136:137], s[22:23], v[8:9] op_sel_hi:[1,0,1]
	v_pk_mul_f32 v[28:29], v[138:139], v[28:29]
	v_min_f32_e32 v136, 0x40e00000, v136
	v_pk_mul_f32 v[32:33], v[32:33], v[28:29]
	v_pk_fma_f32 v[28:29], v[134:135], s[22:23], v[6:7] op_sel_hi:[1,0,1]
	v_min_f32_e32 v137, 0x40e00000, v137
	v_min_f32_e32 v28, 0x40e00000, v28
	v_min_f32_e32 v29, 0x40e00000, v29
	v_pk_mul_f32 v[134:135], v[28:29], s[24:25] op_sel_hi:[1,0]
	v_pk_mul_f32 v[138:139], v[136:137], s[24:25] op_sel_hi:[1,0]
	v_exp_f32_e32 v134, v134
	v_exp_f32_e32 v135, v135
	v_exp_f32_e32 v138, v138
	v_exp_f32_e32 v139, v139
	v_pk_fma_f32 v[130:131], v[130:131], s[22:23], v[2:3] op_sel_hi:[1,0,1]
	v_pk_add_f32 v[134:135], v[134:135], 1.0 op_sel_hi:[1,0]
	v_med3_f32 v130, v130, s87, v189
	v_rcp_f32_e32 v134, v134
	v_rcp_f32_e32 v135, v135
	v_med3_f32 v131, v131, s87, v189
	v_pk_add_f32 v[130:131], v[130:131], 1.0 op_sel_hi:[1,0]
	v_pk_fma_f32 v[132:133], v[132:133], s[22:23], v[4:5] op_sel_hi:[1,0,1]
	v_pk_mul_f32 v[28:29], v[28:29], v[134:135]
	v_med3_f32 v132, v132, s87, v189
	v_pk_mul_f32 v[130:131], v[130:131], v[28:29]
	v_pk_add_f32 v[28:29], v[138:139], 1.0 op_sel_hi:[1,0]
	v_med3_f32 v133, v133, s87, v189
	v_rcp_f32_e32 v28, v28
	v_rcp_f32_e32 v29, v29
	v_pk_fma_f32 v[122:123], v[122:123], s[22:23], v[10:11] op_sel_hi:[1,0,1]
	v_pk_fma_f32 v[118:119], v[118:119], s[22:23], v[6:7] op_sel_hi:[1,0,1]
	v_med3_f32 v122, v122, s87, v189
	v_pk_mul_f32 v[134:135], v[136:137], v[28:29]
	v_mov_b32_e32 v29, v163
	v_cvt_pk_fp8_f32 v29, v130, v131
	v_mov_b32_e32 v28, v163
	v_cvt_pk_fp8_f32 v28, v30, v31
	v_pk_add_f32 v[30:31], v[132:133], 1.0 op_sel_hi:[1,0]
	v_med3_f32 v123, v123, s87, v189
	v_pk_mul_f32 v[30:31], v[30:31], v[134:135]
	v_cvt_pk_fp8_f32 v28, v32, v33 op_sel:[0,0,1]
	v_cvt_pk_fp8_f32 v29, v30, v31 op_sel:[0,0,1]
	v_pk_fma_f32 v[30:31], v[126:127], s[22:23], v[14:15] op_sel_hi:[1,0,1]
	v_pk_fma_f32 v[126:127], v[128:129], s[22:23], v[16:17] op_sel_hi:[1,0,1]
	v_min_f32_e32 v30, 0x40e00000, v30
	v_min_f32_e32 v31, 0x40e00000, v31
	v_pk_mul_f32 v[32:33], v[30:31], s[24:25] op_sel_hi:[1,0]
	v_min_f32_e32 v126, 0x40e00000, v126
	v_exp_f32_e32 v32, v32
	v_exp_f32_e32 v33, v33
	v_min_f32_e32 v127, 0x40e00000, v127
	v_pk_mul_f32 v[128:129], v[126:127], s[24:25] op_sel_hi:[1,0]
	v_min_f32_e32 v118, 0x40e00000, v118
	v_pk_add_f32 v[32:33], v[32:33], 1.0 op_sel_hi:[1,0]
	v_exp_f32_e32 v128, v128
	v_rcp_f32_e32 v32, v32
	v_rcp_f32_e32 v33, v33
	v_exp_f32_e32 v129, v129
	v_min_f32_e32 v119, 0x40e00000, v119
	v_pk_fma_f32 v[120:121], v[120:121], s[22:23], v[8:9] op_sel_hi:[1,0,1]
	v_pk_mul_f32 v[30:31], v[30:31], v[32:33]
	v_pk_add_f32 v[32:33], v[122:123], 1.0 op_sel_hi:[1,0]
	v_pk_fma_f32 v[122:123], v[124:125], s[22:23], v[12:13] op_sel_hi:[1,0,1]
	v_pk_mul_f32 v[30:31], v[32:33], v[30:31]
	v_pk_add_f32 v[32:33], v[128:129], 1.0 op_sel_hi:[1,0]
	v_med3_f32 v122, v122, s87, v189
	v_rcp_f32_e32 v32, v32
	v_rcp_f32_e32 v33, v33
	v_med3_f32 v123, v123, s87, v189
	v_pk_add_f32 v[122:123], v[122:123], 1.0 op_sel_hi:[1,0]
	v_min_f32_e32 v120, 0x40e00000, v120
	v_pk_mul_f32 v[32:33], v[126:127], v[32:33]
	v_min_f32_e32 v121, 0x40e00000, v121
	v_pk_mul_f32 v[32:33], v[122:123], v[32:33]
	v_pk_mul_f32 v[122:123], v[118:119], s[24:25] op_sel_hi:[1,0]
	v_pk_mul_f32 v[124:125], v[120:121], s[24:25] op_sel_hi:[1,0]
	v_exp_f32_e32 v122, v122
	v_exp_f32_e32 v123, v123
	v_exp_f32_e32 v124, v124
	v_exp_f32_e32 v125, v125
	v_pk_fma_f32 v[114:115], v[114:115], s[22:23], v[2:3] op_sel_hi:[1,0,1]
	v_pk_add_f32 v[122:123], v[122:123], 1.0 op_sel_hi:[1,0]
	v_med3_f32 v114, v114, s87, v189
	v_rcp_f32_e32 v122, v122
	v_rcp_f32_e32 v123, v123
	v_med3_f32 v115, v115, s87, v189
	v_pk_add_f32 v[114:115], v[114:115], 1.0 op_sel_hi:[1,0]
	v_pk_fma_f32 v[116:117], v[116:117], s[22:23], v[4:5] op_sel_hi:[1,0,1]
	v_pk_mul_f32 v[118:119], v[118:119], v[122:123]
	v_med3_f32 v116, v116, s87, v189
	v_pk_mul_f32 v[114:115], v[114:115], v[118:119]
	v_pk_add_f32 v[118:119], v[124:125], 1.0 op_sel_hi:[1,0]
	v_med3_f32 v117, v117, s87, v189
	v_rcp_f32_e32 v118, v118
	v_rcp_f32_e32 v119, v119
	v_pk_fma_f32 v[106:107], v[106:107], s[22:23], v[10:11] op_sel_hi:[1,0,1]
	v_pk_fma_f32 v[102:103], v[102:103], s[22:23], v[6:7] op_sel_hi:[1,0,1]
	v_med3_f32 v106, v106, s87, v189
	v_pk_mul_f32 v[118:119], v[120:121], v[118:119]
	v_mov_b32_e32 v121, v163
	v_cvt_pk_fp8_f32 v121, v114, v115
	v_mov_b32_e32 v120, v163
	v_cvt_pk_fp8_f32 v120, v30, v31
	v_pk_add_f32 v[30:31], v[116:117], 1.0 op_sel_hi:[1,0]
	v_med3_f32 v107, v107, s87, v189
	v_pk_mul_f32 v[30:31], v[30:31], v[118:119]
	v_cvt_pk_fp8_f32 v120, v32, v33 op_sel:[0,0,1]
	v_cvt_pk_fp8_f32 v121, v30, v31 op_sel:[0,0,1]
	v_pk_fma_f32 v[30:31], v[110:111], s[22:23], v[14:15] op_sel_hi:[1,0,1]
	v_pk_fma_f32 v[110:111], v[112:113], s[22:23], v[16:17] op_sel_hi:[1,0,1]
	v_min_f32_e32 v30, 0x40e00000, v30
	v_min_f32_e32 v31, 0x40e00000, v31
	v_pk_mul_f32 v[32:33], v[30:31], s[24:25] op_sel_hi:[1,0]
	v_min_f32_e32 v110, 0x40e00000, v110
	v_exp_f32_e32 v32, v32
	v_exp_f32_e32 v33, v33
	v_min_f32_e32 v111, 0x40e00000, v111
	v_pk_mul_f32 v[112:113], v[110:111], s[24:25] op_sel_hi:[1,0]
	v_min_f32_e32 v102, 0x40e00000, v102
	v_pk_add_f32 v[32:33], v[32:33], 1.0 op_sel_hi:[1,0]
	v_exp_f32_e32 v112, v112
	v_rcp_f32_e32 v32, v32
	v_rcp_f32_e32 v33, v33
	v_exp_f32_e32 v113, v113
	v_min_f32_e32 v103, 0x40e00000, v103
	v_pk_fma_f32 v[104:105], v[104:105], s[22:23], v[8:9] op_sel_hi:[1,0,1]
	v_pk_mul_f32 v[30:31], v[30:31], v[32:33]
	v_pk_add_f32 v[32:33], v[106:107], 1.0 op_sel_hi:[1,0]
	v_pk_fma_f32 v[106:107], v[108:109], s[22:23], v[12:13] op_sel_hi:[1,0,1]
	v_pk_mul_f32 v[30:31], v[32:33], v[30:31]
	v_pk_add_f32 v[32:33], v[112:113], 1.0 op_sel_hi:[1,0]
	v_med3_f32 v106, v106, s87, v189
	v_rcp_f32_e32 v32, v32
	v_rcp_f32_e32 v33, v33
	v_med3_f32 v107, v107, s87, v189
	v_pk_add_f32 v[106:107], v[106:107], 1.0 op_sel_hi:[1,0]
	v_min_f32_e32 v104, 0x40e00000, v104
	v_pk_mul_f32 v[32:33], v[110:111], v[32:33]
	v_min_f32_e32 v105, 0x40e00000, v105
	v_pk_mul_f32 v[32:33], v[106:107], v[32:33]
	v_pk_mul_f32 v[106:107], v[102:103], s[24:25] op_sel_hi:[1,0]
	v_pk_mul_f32 v[108:109], v[104:105], s[24:25] op_sel_hi:[1,0]
	v_exp_f32_e32 v106, v106
	v_exp_f32_e32 v107, v107
	v_exp_f32_e32 v108, v108
	v_exp_f32_e32 v109, v109
	v_pk_fma_f32 v[98:99], v[98:99], s[22:23], v[2:3] op_sel_hi:[1,0,1]
	v_pk_add_f32 v[106:107], v[106:107], 1.0 op_sel_hi:[1,0]
	v_med3_f32 v98, v98, s87, v189
	v_rcp_f32_e32 v106, v106
	v_rcp_f32_e32 v107, v107
	v_med3_f32 v99, v99, s87, v189
	v_pk_add_f32 v[98:99], v[98:99], 1.0 op_sel_hi:[1,0]
	v_pk_fma_f32 v[100:101], v[100:101], s[22:23], v[4:5] op_sel_hi:[1,0,1]
	v_pk_mul_f32 v[102:103], v[102:103], v[106:107]
	v_med3_f32 v100, v100, s87, v189
	v_pk_mul_f32 v[98:99], v[98:99], v[102:103]
	v_pk_add_f32 v[102:103], v[108:109], 1.0 op_sel_hi:[1,0]
	v_med3_f32 v101, v101, s87, v189
	v_rcp_f32_e32 v102, v102
	v_rcp_f32_e32 v103, v103
	s_nop 0
	v_pk_mul_f32 v[102:103], v[104:105], v[102:103]
	v_mov_b32_e32 v104, v163
	v_mov_b32_e32 v105, v163
	v_cvt_pk_fp8_f32 v104, v30, v31
	v_cvt_pk_fp8_f32 v105, v98, v99
	v_pk_add_f32 v[30:31], v[100:101], 1.0 op_sel_hi:[1,0]
	v_cvt_pk_fp8_f32 v104, v32, v33 op_sel:[0,0,1]
	v_pk_mul_f32 v[30:31], v[30:31], v[102:103]
	s_nop 0
	v_cvt_pk_fp8_f32 v105, v30, v31 op_sel:[0,0,1]
	v_mov_b32_e32 v246, v20
	v_mov_b32_e32 v247, v21
	v_mov_b32_e32 v248, v28
	v_mov_b32_e32 v249, v29
	s_nop 1
	v_permlane16_swap_b32 v246, v248
	v_permlane16_swap_b32 v247, v249
	global_store_dwordx4 v[18:19], v[246:249], off
	v_mov_b32_e32 v250, v120
	v_mov_b32_e32 v251, v121
	v_mov_b32_e32 v252, v104
	v_mov_b32_e32 v253, v105
	s_nop 1
	v_permlane16_swap_b32 v250, v252
	v_permlane16_swap_b32 v251, v253
	global_store_dwordx4 v[26:27], v[250:253], off
	v_pk_fma_f32 v[20:21], v[94:95], s[22:23], v[14:15] op_sel_hi:[1,0,1]
	v_pk_fma_f32 v[26:27], v[96:97], s[22:23], v[16:17] op_sel_hi:[1,0,1]
	v_min_f32_e32 v20, 0x40e00000, v20
	v_min_f32_e32 v21, 0x40e00000, v21
	v_pk_mul_f32 v[22:23], v[20:21], s[24:25] op_sel_hi:[1,0]
	v_min_f32_e32 v26, 0x40e00000, v26
	v_exp_f32_e32 v22, v22
	v_exp_f32_e32 v23, v23
	v_min_f32_e32 v27, 0x40e00000, v27
	v_pk_mul_f32 v[28:29], v[26:27], s[24:25] op_sel_hi:[1,0]
	v_pk_fma_f32 v[24:25], v[90:91], s[22:23], v[10:11] op_sel_hi:[1,0,1]
	v_pk_add_f32 v[22:23], v[22:23], 1.0 op_sel_hi:[1,0]
	v_exp_f32_e32 v28, v28
	v_rcp_f32_e32 v22, v22
	v_rcp_f32_e32 v23, v23
	v_exp_f32_e32 v29, v29
	v_med3_f32 v24, v24, s87, v189
	v_med3_f32 v25, v25, s87, v189
	v_pk_mul_f32 v[20:21], v[20:21], v[22:23]
	v_pk_add_f32 v[22:23], v[24:25], 1.0 op_sel_hi:[1,0]
	v_pk_fma_f32 v[24:25], v[92:93], s[22:23], v[12:13] op_sel_hi:[1,0,1]
	v_pk_mul_f32 v[20:21], v[22:23], v[20:21]
	v_pk_add_f32 v[22:23], v[28:29], 1.0 op_sel_hi:[1,0]
	v_med3_f32 v24, v24, s87, v189
	v_rcp_f32_e32 v22, v22
	v_rcp_f32_e32 v23, v23
	v_med3_f32 v25, v25, s87, v189
	v_pk_add_f32 v[24:25], v[24:25], 1.0 op_sel_hi:[1,0]
	v_pk_fma_f32 v[30:31], v[88:89], s[22:23], v[8:9] op_sel_hi:[1,0,1]
	v_pk_mul_f32 v[22:23], v[26:27], v[22:23]
	v_min_f32_e32 v30, 0x40e00000, v30
	v_pk_mul_f32 v[22:23], v[24:25], v[22:23]
	v_pk_fma_f32 v[24:25], v[86:87], s[22:23], v[6:7] op_sel_hi:[1,0,1]
	v_min_f32_e32 v31, 0x40e00000, v31
	v_min_f32_e32 v24, 0x40e00000, v24
	v_min_f32_e32 v25, 0x40e00000, v25
	v_pk_mul_f32 v[26:27], v[24:25], s[24:25] op_sel_hi:[1,0]
	v_pk_mul_f32 v[32:33], v[30:31], s[24:25] op_sel_hi:[1,0]
	v_exp_f32_e32 v26, v26
	v_exp_f32_e32 v27, v27
	v_exp_f32_e32 v32, v32
	v_exp_f32_e32 v33, v33
	v_pk_fma_f32 v[28:29], v[82:83], s[22:23], v[2:3] op_sel_hi:[1,0,1]
	v_pk_add_f32 v[26:27], v[26:27], 1.0 op_sel_hi:[1,0]
	v_med3_f32 v28, v28, s87, v189
	v_rcp_f32_e32 v26, v26
	v_rcp_f32_e32 v27, v27
	v_med3_f32 v29, v29, s87, v189
	v_pk_mul_f32 v[24:25], v[24:25], v[26:27]
	v_pk_add_f32 v[26:27], v[28:29], 1.0 op_sel_hi:[1,0]
	v_pk_fma_f32 v[28:29], v[84:85], s[22:23], v[4:5] op_sel_hi:[1,0,1]
	v_pk_mul_f32 v[24:25], v[26:27], v[24:25]
	v_pk_add_f32 v[26:27], v[32:33], 1.0 op_sel_hi:[1,0]
	v_med3_f32 v28, v28, s87, v189
	v_rcp_f32_e32 v26, v26
	v_rcp_f32_e32 v27, v27
	v_med3_f32 v29, v29, s87, v189
	v_pk_mul_f32 v[26:27], v[30:31], v[26:27]
	v_mov_b32_e32 v30, v163
	v_mov_b32_e32 v31, v163
	v_cvt_pk_fp8_f32 v30, v20, v21
	v_cvt_pk_fp8_f32 v31, v24, v25
	v_pk_add_f32 v[20:21], v[28:29], 1.0 op_sel_hi:[1,0]
	v_pk_fma_f32 v[24:25], v[74:75], s[22:23], v[10:11] op_sel_hi:[1,0,1]
	v_pk_mul_f32 v[20:21], v[20:21], v[26:27]
	v_cvt_pk_fp8_f32 v30, v22, v23 op_sel:[0,0,1]
	v_cvt_pk_fp8_f32 v31, v20, v21 op_sel:[0,0,1]
	v_add_co_u32_e32 v20, vcc, s6, v18
	v_pk_fma_f32 v[26:27], v[80:81], s[22:23], v[16:17] op_sel_hi:[1,0,1]
	s_nop 0
	v_addc_co_u32_e32 v21, vcc, 0, v19, vcc
	v_mov_b32_e32 v234, v30
	v_mov_b32_e32 v235, v31
	v_mov_b32_e32 v238, v20
	v_mov_b32_e32 v239, v21
	v_pk_fma_f32 v[20:21], v[78:79], s[22:23], v[14:15] op_sel_hi:[1,0,1]
	v_min_f32_e32 v26, 0x40e00000, v26
	v_min_f32_e32 v20, 0x40e00000, v20
	v_min_f32_e32 v21, 0x40e00000, v21
	v_pk_mul_f32 v[22:23], v[20:21], s[24:25] op_sel_hi:[1,0]
	v_min_f32_e32 v27, 0x40e00000, v27
	v_exp_f32_e32 v22, v22
	v_exp_f32_e32 v23, v23
	v_pk_mul_f32 v[28:29], v[26:27], s[24:25] op_sel_hi:[1,0]
	v_med3_f32 v24, v24, s87, v189
	v_exp_f32_e32 v28, v28
	v_pk_add_f32 v[22:23], v[22:23], 1.0 op_sel_hi:[1,0]
	v_exp_f32_e32 v29, v29
	v_rcp_f32_e32 v22, v22
	v_rcp_f32_e32 v23, v23
	v_med3_f32 v25, v25, s87, v189
	v_pk_fma_f32 v[30:31], v[72:73], s[22:23], v[8:9] op_sel_hi:[1,0,1]
	s_mov_b32 s6, 0x48000
	v_pk_mul_f32 v[20:21], v[20:21], v[22:23]
	v_pk_add_f32 v[22:23], v[24:25], 1.0 op_sel_hi:[1,0]
	v_pk_fma_f32 v[24:25], v[76:77], s[22:23], v[12:13] op_sel_hi:[1,0,1]
	v_pk_mul_f32 v[20:21], v[22:23], v[20:21]
	v_pk_add_f32 v[22:23], v[28:29], 1.0 op_sel_hi:[1,0]
	v_med3_f32 v24, v24, s87, v189
	v_rcp_f32_e32 v22, v22
	v_rcp_f32_e32 v23, v23
	v_med3_f32 v25, v25, s87, v189
	v_pk_add_f32 v[24:25], v[24:25], 1.0 op_sel_hi:[1,0]
	v_min_f32_e32 v30, 0x40e00000, v30
	v_pk_mul_f32 v[22:23], v[26:27], v[22:23]
	v_min_f32_e32 v31, 0x40e00000, v31
	v_pk_mul_f32 v[22:23], v[24:25], v[22:23]
	v_pk_fma_f32 v[24:25], v[70:71], s[22:23], v[6:7] op_sel_hi:[1,0,1]
	v_pk_mul_f32 v[32:33], v[30:31], s[24:25] op_sel_hi:[1,0]
	v_min_f32_e32 v24, 0x40e00000, v24
	v_min_f32_e32 v25, 0x40e00000, v25
	v_pk_mul_f32 v[26:27], v[24:25], s[24:25] op_sel_hi:[1,0]
	v_exp_f32_e32 v32, v32
	v_exp_f32_e32 v26, v26
	v_exp_f32_e32 v27, v27
	v_exp_f32_e32 v33, v33
	v_pk_fma_f32 v[28:29], v[66:67], s[22:23], v[2:3] op_sel_hi:[1,0,1]
	v_pk_add_f32 v[26:27], v[26:27], 1.0 op_sel_hi:[1,0]
	s_nop 0
	v_rcp_f32_e32 v26, v26
	v_rcp_f32_e32 v27, v27
	v_med3_f32 v28, v28, s87, v189
	v_med3_f32 v29, v29, s87, v189
	v_pk_mul_f32 v[24:25], v[24:25], v[26:27]
	v_pk_add_f32 v[26:27], v[28:29], 1.0 op_sel_hi:[1,0]
	v_pk_fma_f32 v[28:29], v[68:69], s[22:23], v[4:5] op_sel_hi:[1,0,1]
	v_pk_mul_f32 v[24:25], v[26:27], v[24:25]
	v_pk_add_f32 v[26:27], v[32:33], 1.0 op_sel_hi:[1,0]
	v_med3_f32 v28, v28, s87, v189
	v_rcp_f32_e32 v26, v26
	v_rcp_f32_e32 v27, v27
	v_med3_f32 v29, v29, s87, v189
	v_pk_mul_f32 v[26:27], v[30:31], v[26:27]
	v_mov_b32_e32 v30, v163
	v_mov_b32_e32 v31, v163
	v_cvt_pk_fp8_f32 v30, v20, v21
	v_cvt_pk_fp8_f32 v31, v24, v25
	v_pk_add_f32 v[20:21], v[28:29], 1.0 op_sel_hi:[1,0]
	v_pk_fma_f32 v[24:25], v[58:59], s[22:23], v[10:11] op_sel_hi:[1,0,1]
	v_pk_mul_f32 v[20:21], v[20:21], v[26:27]
	v_cvt_pk_fp8_f32 v30, v22, v23 op_sel:[0,0,1]
	v_cvt_pk_fp8_f32 v31, v20, v21 op_sel:[0,0,1]
	v_add_co_u32_e32 v20, vcc, s6, v18
	v_pk_fma_f32 v[26:27], v[64:65], s[22:23], v[16:17] op_sel_hi:[1,0,1]
	s_nop 0
	v_addc_co_u32_e32 v21, vcc, 0, v19, vcc
	v_mov_b32_e32 v236, v30
	v_mov_b32_e32 v237, v31
	s_nop 1
	v_permlane16_swap_b32 v234, v236
	v_permlane16_swap_b32 v235, v237
	global_store_dwordx4 v[238:239], v[234:237], off
	v_pk_fma_f32 v[20:21], v[62:63], s[22:23], v[14:15] op_sel_hi:[1,0,1]
	v_min_f32_e32 v26, 0x40e00000, v26
	v_min_f32_e32 v20, 0x40e00000, v20
	v_min_f32_e32 v21, 0x40e00000, v21
	v_pk_mul_f32 v[22:23], v[20:21], s[24:25] op_sel_hi:[1,0]
	v_min_f32_e32 v27, 0x40e00000, v27
	v_exp_f32_e32 v22, v22
	v_exp_f32_e32 v23, v23
	v_pk_mul_f32 v[28:29], v[26:27], s[24:25] op_sel_hi:[1,0]
	v_med3_f32 v24, v24, s87, v189
	v_exp_f32_e32 v28, v28
	v_pk_add_f32 v[22:23], v[22:23], 1.0 op_sel_hi:[1,0]
	v_exp_f32_e32 v29, v29
	v_rcp_f32_e32 v22, v22
	v_rcp_f32_e32 v23, v23
	v_med3_f32 v25, v25, s87, v189
	v_pk_fma_f32 v[30:31], v[56:57], s[22:23], v[8:9] op_sel_hi:[1,0,1]
	s_mov_b32 s6, 0x50000
	v_pk_mul_f32 v[20:21], v[20:21], v[22:23]
	v_pk_add_f32 v[22:23], v[24:25], 1.0 op_sel_hi:[1,0]
	v_pk_fma_f32 v[24:25], v[60:61], s[22:23], v[12:13] op_sel_hi:[1,0,1]
	v_pk_mul_f32 v[20:21], v[22:23], v[20:21]
	v_pk_add_f32 v[22:23], v[28:29], 1.0 op_sel_hi:[1,0]
	v_med3_f32 v24, v24, s87, v189
	v_rcp_f32_e32 v22, v22
	v_rcp_f32_e32 v23, v23
	v_med3_f32 v25, v25, s87, v189
	v_pk_add_f32 v[24:25], v[24:25], 1.0 op_sel_hi:[1,0]
	v_min_f32_e32 v30, 0x40e00000, v30
	v_pk_mul_f32 v[22:23], v[26:27], v[22:23]
	v_min_f32_e32 v31, 0x40e00000, v31
	v_pk_mul_f32 v[22:23], v[24:25], v[22:23]
	v_pk_fma_f32 v[24:25], v[54:55], s[22:23], v[6:7] op_sel_hi:[1,0,1]
	v_pk_mul_f32 v[32:33], v[30:31], s[24:25] op_sel_hi:[1,0]
	v_min_f32_e32 v24, 0x40e00000, v24
	v_min_f32_e32 v25, 0x40e00000, v25
	v_pk_mul_f32 v[26:27], v[24:25], s[24:25] op_sel_hi:[1,0]
	v_exp_f32_e32 v32, v32
	v_exp_f32_e32 v26, v26
	v_exp_f32_e32 v27, v27
	v_exp_f32_e32 v33, v33
	v_pk_fma_f32 v[28:29], v[50:51], s[22:23], v[2:3] op_sel_hi:[1,0,1]
	v_pk_fma_f32 v[14:15], v[46:47], s[22:23], v[14:15] op_sel_hi:[1,0,1]
	v_pk_add_f32 v[26:27], v[26:27], 1.0 op_sel_hi:[1,0]
	v_med3_f32 v28, v28, s87, v189
	v_rcp_f32_e32 v26, v26
	v_rcp_f32_e32 v27, v27
	v_med3_f32 v29, v29, s87, v189
	v_min_f32_e32 v14, 0x40e00000, v14
	v_min_f32_e32 v15, 0x40e00000, v15
	v_pk_mul_f32 v[24:25], v[24:25], v[26:27]
	v_pk_add_f32 v[26:27], v[28:29], 1.0 op_sel_hi:[1,0]
	v_pk_fma_f32 v[28:29], v[52:53], s[22:23], v[4:5] op_sel_hi:[1,0,1]
	v_pk_mul_f32 v[24:25], v[26:27], v[24:25]
	v_pk_add_f32 v[26:27], v[32:33], 1.0 op_sel_hi:[1,0]
	v_med3_f32 v28, v28, s87, v189
	v_rcp_f32_e32 v26, v26
	v_rcp_f32_e32 v27, v27
	v_med3_f32 v29, v29, s87, v189
	v_pk_fma_f32 v[16:17], v[48:49], s[22:23], v[16:17] op_sel_hi:[1,0,1]
	v_pk_fma_f32 v[10:11], v[42:43], s[22:23], v[10:11] op_sel_hi:[1,0,1]
	v_pk_mul_f32 v[26:27], v[30:31], v[26:27]
	v_mov_b32_e32 v30, v163
	v_mov_b32_e32 v31, v163
	v_cvt_pk_fp8_f32 v30, v20, v21
	v_cvt_pk_fp8_f32 v31, v24, v25
	v_pk_add_f32 v[20:21], v[28:29], 1.0 op_sel_hi:[1,0]
	v_min_f32_e32 v16, 0x40e00000, v16
	v_pk_mul_f32 v[20:21], v[20:21], v[26:27]
	v_cvt_pk_fp8_f32 v30, v22, v23 op_sel:[0,0,1]
	v_cvt_pk_fp8_f32 v31, v20, v21 op_sel:[0,0,1]
	v_add_co_u32_e32 v20, vcc, s6, v18
	v_min_f32_e32 v17, 0x40e00000, v17
	s_nop 0
	v_addc_co_u32_e32 v21, vcc, 0, v19, vcc
	v_mov_b32_e32 v240, v30
	v_mov_b32_e32 v241, v31
	v_mov_b32_e32 v244, v20
	v_mov_b32_e32 v245, v21
	v_pk_mul_f32 v[20:21], v[14:15], s[24:25] op_sel_hi:[1,0]
	v_pk_mul_f32 v[22:23], v[16:17], s[24:25] op_sel_hi:[1,0]
	v_exp_f32_e32 v20, v20
	v_exp_f32_e32 v21, v21
	v_exp_f32_e32 v22, v22
	v_exp_f32_e32 v23, v23
	v_med3_f32 v10, v10, s87, v189
	v_pk_add_f32 v[20:21], v[20:21], 1.0 op_sel_hi:[1,0]
	v_med3_f32 v11, v11, s87, v189
	v_rcp_f32_e32 v20, v20
	v_rcp_f32_e32 v21, v21
	v_pk_add_f32 v[10:11], v[10:11], 1.0 op_sel_hi:[1,0]
	v_pk_fma_f32 v[12:13], v[44:45], s[22:23], v[12:13] op_sel_hi:[1,0,1]
	v_pk_fma_f32 v[6:7], v[38:39], s[22:23], v[6:7] op_sel_hi:[1,0,1]
	v_pk_mul_f32 v[14:15], v[14:15], v[20:21]
	v_med3_f32 v12, v12, s87, v189
	v_pk_mul_f32 v[10:11], v[10:11], v[14:15]
	v_pk_add_f32 v[14:15], v[22:23], 1.0 op_sel_hi:[1,0]
	v_med3_f32 v13, v13, s87, v189
	v_rcp_f32_e32 v14, v14
	v_rcp_f32_e32 v15, v15
	v_pk_add_f32 v[12:13], v[12:13], 1.0 op_sel_hi:[1,0]
	v_min_f32_e32 v6, 0x40e00000, v6
	v_min_f32_e32 v7, 0x40e00000, v7
	v_pk_mul_f32 v[14:15], v[16:17], v[14:15]
	v_pk_fma_f32 v[8:9], v[40:41], s[22:23], v[8:9] op_sel_hi:[1,0,1]
	v_pk_mul_f32 v[12:13], v[12:13], v[14:15]
	v_pk_mul_f32 v[14:15], v[6:7], s[24:25] op_sel_hi:[1,0]
	v_min_f32_e32 v8, 0x40e00000, v8
	v_exp_f32_e32 v14, v14
	v_exp_f32_e32 v15, v15
	v_min_f32_e32 v9, 0x40e00000, v9
	v_pk_mul_f32 v[16:17], v[8:9], s[24:25] op_sel_hi:[1,0]
	v_pk_fma_f32 v[2:3], v[34:35], s[22:23], v[2:3] op_sel_hi:[1,0,1]
	v_pk_add_f32 v[14:15], v[14:15], 1.0 op_sel_hi:[1,0]
	v_exp_f32_e32 v16, v16
	v_rcp_f32_e32 v14, v14
	v_rcp_f32_e32 v15, v15
	v_exp_f32_e32 v17, v17
	v_med3_f32 v2, v2, s87, v189
	v_med3_f32 v3, v3, s87, v189
	v_pk_mul_f32 v[6:7], v[6:7], v[14:15]
	v_pk_add_f32 v[2:3], v[2:3], 1.0 op_sel_hi:[1,0]
	v_pk_fma_f32 v[4:5], v[36:37], s[22:23], v[4:5] op_sel_hi:[1,0,1]
	v_pk_mul_f32 v[2:3], v[2:3], v[6:7]
	v_pk_add_f32 v[6:7], v[16:17], 1.0 op_sel_hi:[1,0]
	v_med3_f32 v4, v4, s87, v189
	v_rcp_f32_e32 v6, v6
	v_rcp_f32_e32 v7, v7
	v_med3_f32 v5, v5, s87, v189
	v_pk_mul_f32 v[6:7], v[8:9], v[6:7]
	v_mov_b32_e32 v8, v163
	v_mov_b32_e32 v9, v163
	v_cvt_pk_fp8_f32 v8, v10, v11
	v_cvt_pk_fp8_f32 v9, v2, v3
	v_pk_add_f32 v[2:3], v[4:5], 1.0 op_sel_hi:[1,0]
	v_cvt_pk_fp8_f32 v8, v12, v13 op_sel:[0,0,1]
	v_pk_mul_f32 v[2:3], v[2:3], v[6:7]
	s_nop 0
	v_cvt_pk_fp8_f32 v9, v2, v3 op_sel:[0,0,1]
	v_add_co_u32_e32 v2, vcc, 0x58000, v18
	s_nop 1
	v_addc_co_u32_e32 v3, vcc, 0, v19, vcc
	s_andn2_b64 vcc, exec, s[4:5]
	s_mov_b64 s[4:5], -1
	v_mov_b32_e32 v242, v8
	v_mov_b32_e32 v243, v9
	s_nop 1
	v_permlane16_swap_b32 v240, v242
	v_permlane16_swap_b32 v241, v243
	global_store_dwordx4 v[244:245], v[240:243], off
	s_cbranch_vccnz .LBB0_1348
	s_andn2_b64 vcc, exec, s[12:13]
	s_cbranch_vccnz .LBB0_1347
	s_barrier
	s_branch .LBB0_1347
